# speedup vs baseline: 1.0060x; 1.0009x over previous
.LBB1_9:
	v_add_u32_e32 v182, s20, v209
	ds_read_b64_tr_b16 v[178:179], v182 offset:24576
	ds_read_b64_tr_b16 v[180:181], v182 offset:25088
	s_waitcnt lgkmcnt(9)
	v_mfma_f32_32x32x16_f16 v[98:113], v[174:177], v[142:145], v[34:49]
	s_mov_b64 s[2:3], 0
	v_add_f32_e32 v82, v66, v67
	v_add_f32_e32 v82, v68, v82
	v_add_f32_e32 v82, v69, v82
	v_add_f32_e32 v82, v70, v82
	v_add_f32_e32 v82, v71, v82
	v_cvt_pk_f16_f32 v134, v66, v67
	v_cvt_pk_f16_f32 v135, v68, v69
	ds_read_b64_tr_b16 v[174:175], v182 offset:28672
	ds_read_b64_tr_b16 v[176:177], v182 offset:29184
	v_add_f32_e32 v66, v72, v82
	s_waitcnt lgkmcnt(10)
	v_mfma_f32_32x32x16_f16 v[82:97], v[170:173], v[142:145], v[34:49]
	v_add_f32_e32 v66, v73, v66
	v_add_f32_e32 v66, v74, v66
	v_add_f32_e32 v66, v75, v66
	v_cvt_pk_f16_f32 v136, v70, v71
	v_cvt_pk_f16_f32 v137, v72, v73
	ds_read_b64_tr_b16 v[170:171], v182 offset:25600
	ds_read_b64_tr_b16 v[172:173], v182 offset:26112
	s_waitcnt lgkmcnt(11)
	v_mfma_f32_32x32x16_f16 v[98:113], v[166:169], v[138:141], v[98:113]
	v_add_f32_e32 v66, v76, v66
	v_add_f32_e32 v66, v77, v66
	v_add_f32_e32 v66, v78, v66
	v_add_f32_e32 v66, v79, v66
	v_cvt_pk_f16_f32 v126, v74, v75
	v_cvt_pk_f16_f32 v127, v76, v77
	ds_read_b64_tr_b16 v[74:75], v182 offset:29696
	ds_read_b64_tr_b16 v[76:77], v182 offset:30208
	s_waitcnt lgkmcnt(12)
	v_mfma_f32_32x32x16_f16 v[82:97], v[162:165], v[138:141], v[82:97]
	v_add_f32_e32 v66, v80, v66
	v_add_f32_e32 v66, v81, v66
	v_add_f32_e32 v66, v50, v66
	v_add_f32_e32 v66, v51, v66
	v_cvt_pk_f16_f32 v128, v78, v79
	v_cvt_pk_f16_f32 v129, v80, v81
	ds_read_b64_tr_b16 v[70:71], v182 offset:26624
	ds_read_b64_tr_b16 v[72:73], v182 offset:27136
	s_waitcnt lgkmcnt(13)
	v_mfma_f32_32x32x16_f16 v[98:113], v[158:161], v[130:133], v[98:113]
	v_add_f32_e32 v66, v52, v66
	v_add_f32_e32 v66, v53, v66
	v_add_f32_e32 v66, v54, v66
	v_add_f32_e32 v78, v55, v66
	v_cvt_pk_f16_f32 v118, v50, v51
	v_cvt_pk_f16_f32 v119, v52, v53
	ds_read_b64_tr_b16 v[66:67], v182 offset:30720
	ds_read_b64_tr_b16 v[68:69], v182 offset:31232
	s_waitcnt lgkmcnt(14)
	v_mfma_f32_32x32x16_f16 v[82:97], v[154:157], v[130:133], v[82:97]
	v_add_f32_e32 v50, v56, v78
	v_add_f32_e32 v50, v57, v50
	v_add_f32_e32 v50, v58, v50
	v_add_f32_e32 v50, v59, v50
	v_cvt_pk_f16_f32 v120, v54, v55
	v_cvt_pk_f16_f32 v121, v56, v57
	ds_read_b64_tr_b16 v[54:55], v182 offset:27648
	ds_read_b64_tr_b16 v[56:57], v182 offset:28160
	s_waitcnt lgkmcnt(14)
	v_mfma_f32_32x32x16_f16 v[98:113], v[150:153], v[122:125], v[98:113]
	v_add_f32_e32 v50, v60, v50
	v_add_f32_e32 v50, v61, v50
	v_add_f32_e32 v50, v62, v50
	v_add_f32_e32 v78, v63, v50
	v_cvt_pk_f16_f32 v114, v58, v59
	v_cvt_pk_f16_f32 v115, v60, v61
	ds_read_b64_tr_b16 v[50:51], v182 offset:31744
	ds_read_b64_tr_b16 v[52:53], v182 offset:32256
	v_mfma_f32_32x32x16_f16 v[82:97], v[146:149], v[122:125], v[82:97]
	v_add_f32_e32 v58, v64, v78
	v_add_f32_e32 v58, v65, v58
	v_cvt_pk_f16_f32 v116, v62, v63
	v_cvt_pk_f16_f32 v117, v64, v65
	v_max_f32_e32 v59, v98, v99
	v_max3_f32 v60, v100, v101, v102
	v_max3_f32 v59, v59, v103, v104
	v_max3_f32 v60, v60, v105, v106
	v_max3_f32 v59, v59, v107, v108
	v_max3_f32 v60, v60, v109, v110
	v_max3_f32 v59, v59, v111, v112
	v_add_f32_e32 v182, v203, v58
	v_max3_f32 v60, v60, v113, v82
	v_max3_f32 v59, v59, v83, v84
	v_max3_f32 v60, v60, v85, v86
	v_max3_f32 v59, v59, v87, v88
	v_max3_f32 v60, v60, v89, v90
	v_max3_f32 v59, v59, v91, v92
	v_max3_f32 v60, v60, v93, v94
	v_max3_f32 v59, v59, v95, v96
	v_max3_f32 v58, v59, v60, v97
	v_cmp_lt_f32_e32 vcc, s23, v58
	s_cmp_lg_u64 vcc, 0
	s_cbranch_scc1 .LBB1_17
.LBB1_10:
	s_add_u32 s52, s16, 0xffffe000
	s_addc_u32 s53, s17, -1
	s_waitcnt lgkmcnt(14)
	v_mfma_f32_32x32x16_f16 v[2:17], v[134:137], v[178:181], v[2:17]
	v_exp_f32_e32 v98, v98
	v_exp_f32_e32 v99, v99
	v_exp_f32_e32 v100, v100
	v_exp_f32_e32 v101, v101
	s_add_i32 s54, s24, s39
	s_mov_b32 m0, s54
	s_waitcnt lgkmcnt(12)
	v_mfma_f32_32x32x16_f16 v[18:33], v[134:137], v[174:177], v[18:33]
	global_load_lds_dwordx4 v211, s[52:53]
	v_exp_f32_e32 v102, v102
	v_exp_f32_e32 v103, v103
	v_exp_f32_e32 v104, v104
	v_exp_f32_e32 v105, v105
	v_add_u32_e32 v62, s22, v200
	ds_read_b128 v[58:61], v62
	ds_read_b128 v[146:149], v62 offset:512
	s_add_i32 s54, s22, s40
	s_mov_b32 m0, s54
	s_waitcnt lgkmcnt(12)
	v_mfma_f32_32x32x16_f16 v[2:17], v[126:129], v[170:173], v[2:17]
	global_load_lds_dwordx4 v211, s[18:19]
	v_exp_f32_e32 v106, v106
	v_exp_f32_e32 v107, v107
	v_exp_f32_e32 v108, v108
	v_exp_f32_e32 v109, v109
	ds_read_b128 v[178:181], v62 offset:2048
	ds_read_b128 v[170:173], v62 offset:2560
	s_waitcnt lgkmcnt(12)
	v_mfma_f32_32x32x16_f16 v[18:33], v[126:129], v[74:77], v[18:33]
	v_exp_f32_e32 v110, v110
	v_exp_f32_e32 v111, v111
	v_exp_f32_e32 v112, v112
	v_exp_f32_e32 v113, v113
	ds_read_b128 v[174:177], v62 offset:4096
	ds_read_b128 v[162:165], v62 offset:4608
	s_waitcnt lgkmcnt(12)
	v_mfma_f32_32x32x16_f16 v[2:17], v[118:121], v[70:73], v[2:17]
	v_exp_f32_e32 v82, v82
	v_exp_f32_e32 v83, v83
	v_exp_f32_e32 v84, v84
	v_exp_f32_e32 v85, v85
	ds_read_b128 v[166:169], v62 offset:6144
	ds_read_b128 v[158:161], v62 offset:6656
	s_waitcnt lgkmcnt(12)
	v_mfma_f32_32x32x16_f16 v[18:33], v[118:121], v[66:69], v[18:33]
	v_exp_f32_e32 v86, v86
	v_exp_f32_e32 v87, v87
	v_exp_f32_e32 v88, v88
	v_exp_f32_e32 v89, v89
	s_waitcnt lgkmcnt(10)
	v_mfma_f32_32x32x16_f16 v[2:17], v[114:117], v[54:57], v[2:17]
	v_exp_f32_e32 v90, v90
	v_exp_f32_e32 v91, v91
	v_exp_f32_e32 v92, v92
	v_exp_f32_e32 v93, v93
	s_waitcnt lgkmcnt(8)
	v_mfma_f32_32x32x16_f16 v[18:33], v[114:117], v[50:53], v[18:33]
	v_exp_f32_e32 v94, v94
	v_exp_f32_e32 v95, v95
	v_exp_f32_e32 v96, v96
	v_exp_f32_e32 v97, v97
	s_waitcnt vmcnt(2) lgkmcnt(0)
	s_barrier
	s_andn2_b64 vcc, exec, s[2:3]
	v_add_u32_e32 v202, s38, v212
	s_cbranch_vccnz .LBB1_12
	s_waitcnt lgkmcnt(0)
	ds_read_b128 v[50:53], v202 offset:49248
	ds_read_b128 v[54:57], v202 offset:49216
	ds_read_b128 v[62:65], v202 offset:49184
	ds_read_b128 v[66:69], v202 offset:49152
	s_waitcnt lgkmcnt(3)
	v_pk_mul_f32 v[14:15], v[14:15], v[50:51]
	s_waitcnt lgkmcnt(2)
	v_pk_mul_f32 v[10:11], v[10:11], v[54:55]
	s_waitcnt lgkmcnt(1)
	v_pk_mul_f32 v[6:7], v[6:7], v[62:63]
	v_pk_mul_f32 v[16:17], v[16:17], v[52:53]
	v_pk_mul_f32 v[12:13], v[12:13], v[56:57]
	v_pk_mul_f32 v[8:9], v[8:9], v[64:65]
	s_waitcnt lgkmcnt(0)
	v_pk_mul_f32 v[4:5], v[4:5], v[68:69]
	v_pk_mul_f32 v[2:3], v[2:3], v[66:67]
	v_pk_mul_f32 v[30:31], v[30:31], v[50:51]
	v_pk_mul_f32 v[26:27], v[26:27], v[54:55]
	v_pk_mul_f32 v[22:23], v[22:23], v[62:63]
	v_pk_mul_f32 v[32:33], v[32:33], v[52:53]
	v_pk_mul_f32 v[28:29], v[28:29], v[56:57]
	v_pk_mul_f32 v[24:25], v[24:25], v[64:65]
	v_pk_mul_f32 v[20:21], v[20:21], v[68:69]
	v_pk_mul_f32 v[18:19], v[18:19], v[66:67]
.LBB1_12:
	s_add_i32 s2, s22, 0x2000
	s_cmpk_lg_i32 s22, 0x4000
	s_cselect_b32 s43, s2, 0
	v_add_u32_e32 v183, s24, v209
	ds_read_b64_tr_b16 v[154:155], v183 offset:24576
	ds_read_b64_tr_b16 v[156:157], v183 offset:25088
	s_waitcnt lgkmcnt(9)
	v_mfma_f32_32x32x16_f16 v[66:81], v[58:61], v[142:145], v[34:49]
	s_mov_b64 s[2:3], 0
	v_add_f32_e32 v50, v98, v99
	v_add_f32_e32 v50, v100, v50
	v_add_f32_e32 v50, v101, v50
	v_add_f32_e32 v50, v102, v50
	v_add_f32_e32 v50, v103, v50
	v_cvt_pk_f16_f32 v134, v98, v99
	v_cvt_pk_f16_f32 v135, v100, v101
	ds_read_b64_tr_b16 v[150:151], v183 offset:28672
	ds_read_b64_tr_b16 v[152:153], v183 offset:29184
	v_add_f32_e32 v50, v104, v50
	v_add_f32_e32 v50, v105, v50
	v_add_f32_e32 v50, v106, v50
	v_add_f32_e32 v98, v107, v50
	s_waitcnt lgkmcnt(10)
	v_mfma_f32_32x32x16_f16 v[50:65], v[146:149], v[142:145], v[34:49]
	v_cvt_pk_f16_f32 v136, v102, v103
	v_cvt_pk_f16_f32 v137, v104, v105
	ds_read_b64_tr_b16 v[146:147], v183 offset:25600
	ds_read_b64_tr_b16 v[148:149], v183 offset:26112
	s_waitcnt lgkmcnt(11)
	v_mfma_f32_32x32x16_f16 v[66:81], v[178:181], v[138:141], v[66:81]
	v_add_f32_e32 v98, v108, v98
	v_add_f32_e32 v98, v109, v98
	v_add_f32_e32 v98, v110, v98
	v_add_f32_e32 v98, v111, v98
	v_cvt_pk_f16_f32 v126, v106, v107
	v_cvt_pk_f16_f32 v127, v108, v109
	ds_read_b64_tr_b16 v[106:107], v183 offset:29696
	ds_read_b64_tr_b16 v[108:109], v183 offset:30208
	s_waitcnt lgkmcnt(12)
	v_mfma_f32_32x32x16_f16 v[50:65], v[170:173], v[138:141], v[50:65]
	v_add_f32_e32 v98, v112, v98
	v_add_f32_e32 v98, v113, v98
	v_add_f32_e32 v98, v82, v98
	v_add_f32_e32 v98, v83, v98
	v_cvt_pk_f16_f32 v128, v110, v111
	v_cvt_pk_f16_f32 v129, v112, v113
	ds_read_b64_tr_b16 v[102:103], v183 offset:26624
	ds_read_b64_tr_b16 v[104:105], v183 offset:27136
	s_waitcnt lgkmcnt(13)
	v_mfma_f32_32x32x16_f16 v[66:81], v[174:177], v[130:133], v[66:81]
	v_add_f32_e32 v98, v84, v98
	v_add_f32_e32 v98, v85, v98
	v_add_f32_e32 v98, v86, v98
	v_add_f32_e32 v110, v87, v98
	v_cvt_pk_f16_f32 v118, v82, v83
	v_cvt_pk_f16_f32 v119, v84, v85
	ds_read_b64_tr_b16 v[98:99], v183 offset:30720
	ds_read_b64_tr_b16 v[100:101], v183 offset:31232
	s_waitcnt lgkmcnt(14)
	v_mfma_f32_32x32x16_f16 v[50:65], v[162:165], v[130:133], v[50:65]
	v_add_f32_e32 v82, v88, v110
	v_add_f32_e32 v82, v89, v82
	v_add_f32_e32 v82, v90, v82
	v_add_f32_e32 v82, v91, v82
	v_cvt_pk_f16_f32 v120, v86, v87
	v_cvt_pk_f16_f32 v121, v88, v89
	ds_read_b64_tr_b16 v[86:87], v183 offset:27648
	ds_read_b64_tr_b16 v[88:89], v183 offset:28160
	s_waitcnt lgkmcnt(14)
	v_mfma_f32_32x32x16_f16 v[66:81], v[166:169], v[122:125], v[66:81]
	v_add_f32_e32 v82, v92, v82
	v_add_f32_e32 v82, v93, v82
	v_add_f32_e32 v82, v94, v82
	v_add_f32_e32 v110, v95, v82
	v_cvt_pk_f16_f32 v114, v90, v91
	v_cvt_pk_f16_f32 v115, v92, v93
	ds_read_b64_tr_b16 v[82:83], v183 offset:31744
	ds_read_b64_tr_b16 v[84:85], v183 offset:32256
	v_mfma_f32_32x32x16_f16 v[50:65], v[158:161], v[122:125], v[50:65]
	v_add_f32_e32 v90, v96, v110
	v_add_f32_e32 v90, v97, v90
	v_cvt_pk_f16_f32 v116, v94, v95
	v_cvt_pk_f16_f32 v117, v96, v97
	v_max_f32_e32 v91, v66, v67
	v_max3_f32 v92, v68, v69, v70
	v_max3_f32 v91, v91, v71, v72
	v_max3_f32 v92, v92, v73, v74
	v_max3_f32 v91, v91, v75, v76
	v_max3_f32 v92, v92, v77, v78
	v_max3_f32 v91, v91, v79, v80
	v_add_f32_e32 v203, v182, v90
	v_max3_f32 v92, v92, v81, v50
	v_max3_f32 v91, v91, v51, v52
	v_max3_f32 v92, v92, v53, v54
	v_max3_f32 v91, v91, v55, v56
	v_max3_f32 v92, v92, v57, v58
	v_max3_f32 v91, v91, v59, v60
	v_max3_f32 v92, v92, v61, v62
	v_max3_f32 v91, v91, v63, v64
	v_max3_f32 v90, v91, v92, v65
	v_cmp_lt_f32_e32 vcc, s23, v90
	s_cmp_lg_u64 vcc, 0
	s_cbranch_scc1 .LBB1_20
.LBB1_13:
	s_add_u32 s52, s18, 0x2000
	s_addc_u32 s53, s19, 0
	s_waitcnt lgkmcnt(14)
	v_mfma_f32_32x32x16_f16 v[2:17], v[134:137], v[154:157], v[2:17]
	v_exp_f32_e32 v66, v66
	v_exp_f32_e32 v67, v67
	v_exp_f32_e32 v68, v68
	v_exp_f32_e32 v69, v69
	s_add_i32 s54, s22, s39
	s_mov_b32 m0, s54
	s_waitcnt lgkmcnt(12)
	v_mfma_f32_32x32x16_f16 v[18:33], v[134:137], v[150:153], v[18:33]
	global_load_lds_dwordx4 v211, s[16:17]
	v_exp_f32_e32 v70, v70
	v_exp_f32_e32 v71, v71
	v_exp_f32_e32 v72, v72
	v_exp_f32_e32 v73, v73
	v_add_u32_e32 v90, s43, v200
	ds_read_b128 v[174:177], v90
	ds_read_b128 v[170:173], v90 offset:512
	s_add_i32 s54, s43, s40
	s_mov_b32 m0, s54
	s_waitcnt lgkmcnt(12)
	v_mfma_f32_32x32x16_f16 v[2:17], v[126:129], v[146:149], v[2:17]
	global_load_lds_dwordx4 v211, s[52:53]
	v_exp_f32_e32 v74, v74
	v_exp_f32_e32 v75, v75
	v_exp_f32_e32 v76, v76
	v_exp_f32_e32 v77, v77
	ds_read_b128 v[166:169], v90 offset:2048
	ds_read_b128 v[162:165], v90 offset:2560
	s_waitcnt lgkmcnt(12)
	v_mfma_f32_32x32x16_f16 v[18:33], v[126:129], v[106:109], v[18:33]
	v_exp_f32_e32 v78, v78
	v_exp_f32_e32 v79, v79
	v_exp_f32_e32 v80, v80
	v_exp_f32_e32 v81, v81
	ds_read_b128 v[158:161], v90 offset:4096
	ds_read_b128 v[154:157], v90 offset:4608
	s_waitcnt lgkmcnt(12)
	v_mfma_f32_32x32x16_f16 v[2:17], v[118:121], v[102:105], v[2:17]
	v_exp_f32_e32 v50, v50
	v_exp_f32_e32 v51, v51
	v_exp_f32_e32 v52, v52
	v_exp_f32_e32 v53, v53
	ds_read_b128 v[150:153], v90 offset:6144
	ds_read_b128 v[146:149], v90 offset:6656
	s_waitcnt lgkmcnt(12)
	v_mfma_f32_32x32x16_f16 v[18:33], v[118:121], v[98:101], v[18:33]
	v_exp_f32_e32 v54, v54
	v_exp_f32_e32 v55, v55
	v_exp_f32_e32 v56, v56
	v_exp_f32_e32 v57, v57
	s_waitcnt lgkmcnt(10)
	v_mfma_f32_32x32x16_f16 v[2:17], v[114:117], v[86:89], v[2:17]
	v_exp_f32_e32 v58, v58
	v_exp_f32_e32 v59, v59
	v_exp_f32_e32 v60, v60
	v_exp_f32_e32 v61, v61
	s_waitcnt lgkmcnt(8)
	v_mfma_f32_32x32x16_f16 v[18:33], v[114:117], v[82:85], v[18:33]
	v_exp_f32_e32 v62, v62
	v_exp_f32_e32 v63, v63
	v_exp_f32_e32 v64, v64
	v_exp_f32_e32 v65, v65
	s_waitcnt vmcnt(2) lgkmcnt(0)
	s_barrier
	s_andn2_b64 vcc, exec, s[2:3]
	s_cbranch_vccnz .LBB1_15
	s_waitcnt lgkmcnt(0)
	ds_read_b128 v[82:85], v202 offset:49248
	ds_read_b128 v[86:89], v202 offset:49216
	ds_read_b128 v[90:93], v202 offset:49184
	ds_read_b128 v[94:97], v202 offset:49152
	s_waitcnt lgkmcnt(3)
	v_pk_mul_f32 v[14:15], v[14:15], v[82:83]
	s_waitcnt lgkmcnt(2)
	v_pk_mul_f32 v[10:11], v[10:11], v[86:87]
	s_waitcnt lgkmcnt(1)
	v_pk_mul_f32 v[6:7], v[6:7], v[90:91]
	v_pk_mul_f32 v[16:17], v[16:17], v[84:85]
	v_pk_mul_f32 v[12:13], v[12:13], v[88:89]
	v_pk_mul_f32 v[8:9], v[8:9], v[92:93]
	s_waitcnt lgkmcnt(0)
	v_pk_mul_f32 v[4:5], v[4:5], v[96:97]
	v_pk_mul_f32 v[2:3], v[2:3], v[94:95]
	v_pk_mul_f32 v[30:31], v[30:31], v[82:83]
	v_pk_mul_f32 v[26:27], v[26:27], v[86:87]
	v_pk_mul_f32 v[22:23], v[22:23], v[90:91]
	v_pk_mul_f32 v[32:33], v[32:33], v[84:85]
	v_pk_mul_f32 v[28:29], v[28:29], v[88:89]
	v_pk_mul_f32 v[24:25], v[24:25], v[92:93]
	v_pk_mul_f32 v[20:21], v[20:21], v[96:97]
	v_pk_mul_f32 v[18:19], v[18:19], v[94:95]

.LBB1_17:
	s_mov_b64 s[2:3], -1
	v_mov_b32_e32 v59, v58
	s_nop 1
	v_permlane32_swap_b32_e32 v58, v59
	v_max_f32_e32 v58, v58, v59
	v_max_f32_e32 v34, v58, v58
	v_max_f32_e32 v58, 0, v34
	v_exp_f32_e64 v59, -v58
	v_add_f32_e32 v199, v199, v58
	v_xor_b32_e32 v34, 0x80000000, v199
	v_mov_b32_e32 v35, v34
	v_mov_b32_e32 v36, v34
	v_mov_b32_e32 v37, v34
	v_mov_b32_e32 v38, v34
	v_mov_b32_e32 v39, v34
	v_mov_b32_e32 v40, v34
	v_mov_b32_e32 v41, v34
	v_mov_b32_e32 v42, v34
	v_mov_b32_e32 v43, v34
	v_mov_b32_e32 v44, v34
	v_mov_b32_e32 v45, v34
	v_mov_b32_e32 v46, v34
	v_mov_b32_e32 v47, v34
	v_mov_b32_e32 v48, v34
	v_mov_b32_e32 v49, v34
	s_and_saveexec_b64 s[20:21], s[0:1]
	ds_write_b32 v198, v59 offset:49152
	s_or_b64 exec, exec, s[20:21]
	v_sub_f32_e32 v113, v113, v58
	v_sub_f32_e32 v112, v112, v58
	v_sub_f32_e32 v111, v111, v58
	v_sub_f32_e32 v110, v110, v58
	v_sub_f32_e32 v109, v109, v58
	v_sub_f32_e32 v108, v108, v58
	v_sub_f32_e32 v107, v107, v58
	v_sub_f32_e32 v106, v106, v58
	v_sub_f32_e32 v105, v105, v58
	v_sub_f32_e32 v104, v104, v58
	v_sub_f32_e32 v103, v103, v58
	v_sub_f32_e32 v102, v102, v58
	v_sub_f32_e32 v101, v101, v58
	v_sub_f32_e32 v100, v100, v58
	v_sub_f32_e32 v99, v99, v58
	v_sub_f32_e32 v98, v98, v58
	v_sub_f32_e32 v97, v97, v58
	v_sub_f32_e32 v96, v96, v58
	v_sub_f32_e32 v95, v95, v58
	v_sub_f32_e32 v94, v94, v58
	v_sub_f32_e32 v93, v93, v58
	v_sub_f32_e32 v92, v92, v58
	v_sub_f32_e32 v91, v91, v58
	v_sub_f32_e32 v90, v90, v58
	v_sub_f32_e32 v89, v89, v58
	v_sub_f32_e32 v88, v88, v58
	v_sub_f32_e32 v87, v87, v58
	v_sub_f32_e32 v86, v86, v58
	v_sub_f32_e32 v85, v85, v58
	v_sub_f32_e32 v84, v84, v58
	v_sub_f32_e32 v83, v83, v58
	v_sub_f32_e32 v82, v82, v58
	v_mul_f32_e32 v182, v182, v59
	s_branch .LBB1_10
.LBB1_20:
	s_mov_b64 s[2:3], -1
	v_mov_b32_e32 v91, v90
	s_nop 1
	v_permlane32_swap_b32_e32 v90, v91
	v_max_f32_e32 v90, v90, v91
	v_max_f32_e32 v34, v90, v90
	v_max_f32_e32 v90, 0, v34
	v_exp_f32_e64 v91, -v90
	v_add_f32_e32 v199, v199, v90
	v_xor_b32_e32 v34, 0x80000000, v199
	v_mov_b32_e32 v35, v34
	v_mov_b32_e32 v36, v34
	v_mov_b32_e32 v37, v34
	v_mov_b32_e32 v38, v34
	v_mov_b32_e32 v39, v34
	v_mov_b32_e32 v40, v34
	v_mov_b32_e32 v41, v34
	v_mov_b32_e32 v42, v34
	v_mov_b32_e32 v43, v34
	v_mov_b32_e32 v44, v34
	v_mov_b32_e32 v45, v34
	v_mov_b32_e32 v46, v34
	v_mov_b32_e32 v47, v34
	v_mov_b32_e32 v48, v34
	v_mov_b32_e32 v49, v34
	s_and_saveexec_b64 s[20:21], s[0:1]
	ds_write_b32 v198, v91 offset:49152
	s_or_b64 exec, exec, s[20:21]
	v_sub_f32_e32 v81, v81, v90
	v_sub_f32_e32 v80, v80, v90
	v_sub_f32_e32 v79, v79, v90
	v_sub_f32_e32 v78, v78, v90
	v_sub_f32_e32 v77, v77, v90
	v_sub_f32_e32 v76, v76, v90
	v_sub_f32_e32 v75, v75, v90
	v_sub_f32_e32 v74, v74, v90
	v_sub_f32_e32 v73, v73, v90
	v_sub_f32_e32 v72, v72, v90
	v_sub_f32_e32 v71, v71, v90
	v_sub_f32_e32 v70, v70, v90
	v_sub_f32_e32 v69, v69, v90
	v_sub_f32_e32 v68, v68, v90
	v_sub_f32_e32 v67, v67, v90
	v_sub_f32_e32 v66, v66, v90
	v_sub_f32_e32 v65, v65, v90
	v_sub_f32_e32 v64, v64, v90
	v_sub_f32_e32 v63, v63, v90
	v_sub_f32_e32 v62, v62, v90
	v_sub_f32_e32 v61, v61, v90
	v_sub_f32_e32 v60, v60, v90
	v_sub_f32_e32 v59, v59, v90
	v_sub_f32_e32 v58, v58, v90
	v_sub_f32_e32 v57, v57, v90
	v_sub_f32_e32 v56, v56, v90
	v_sub_f32_e32 v55, v55, v90
	v_sub_f32_e32 v54, v54, v90
	v_sub_f32_e32 v53, v53, v90
	v_sub_f32_e32 v52, v52, v90
	v_sub_f32_e32 v51, v51, v90
	v_sub_f32_e32 v50, v50, v90
	v_mul_f32_e32 v203, v203, v91
	s_branch .LBB1_13

.LBB1_87:
	v_add_u32_e32 v65, s6, v251
	ds_read_b64_tr_b16 v[192:193], v65
	ds_read_b64_tr_b16 v[194:195], v65 offset:512
	s_waitcnt lgkmcnt(9)
	v_mfma_f32_32x32x16_f16 v[112:127], v[188:191], v[140:143], v[32:47]
	s_mov_b64 s[6:7], 0
	v_add_f32_e32 v66, v80, v81
	v_add_f32_e32 v66, v82, v66
	v_add_f32_e32 v66, v83, v66
	v_add_f32_e32 v66, v84, v66
	v_add_f32_e32 v66, v85, v66
	v_cvt_pk_f16_f32 v156, v80, v81
	v_cvt_pk_f16_f32 v157, v82, v83
	ds_read_b64_tr_b16 v[188:189], v65 offset:4096
	ds_read_b64_tr_b16 v[190:191], v65 offset:4608
	s_waitcnt lgkmcnt(10)
	v_mfma_f32_32x32x16_f16 v[96:111], v[184:187], v[140:143], v[32:47]
	v_add_f32_e32 v66, v86, v66
	v_add_f32_e32 v66, v87, v66
	v_add_f32_e32 v66, v88, v66
	v_add_f32_e32 v66, v89, v66
	v_cvt_pk_f16_f32 v158, v84, v85
	v_cvt_pk_f16_f32 v159, v86, v87
	ds_read_b64_tr_b16 v[78:79], v65 offset:1024
	ds_read_b64_tr_b16 v[80:81], v65 offset:1536
	s_waitcnt lgkmcnt(11)
	v_mfma_f32_32x32x16_f16 v[112:127], v[180:183], v[136:139], v[112:127]
	v_add_f32_e32 v66, v90, v66
	v_add_f32_e32 v66, v91, v66
	v_add_f32_e32 v66, v92, v66
	v_add_f32_e32 v66, v93, v66
	v_cvt_pk_f16_f32 v152, v88, v89
	v_cvt_pk_f16_f32 v153, v90, v91
	ds_read_b64_tr_b16 v[74:75], v65 offset:5120
	ds_read_b64_tr_b16 v[76:77], v65 offset:5632
	s_waitcnt lgkmcnt(12)
	v_mfma_f32_32x32x16_f16 v[96:111], v[176:179], v[136:139], v[96:111]
	v_add_f32_e32 v66, v94, v66
	v_add_f32_e32 v66, v95, v66
	v_add_f32_e32 v66, v48, v66
	v_add_f32_e32 v66, v49, v66
	v_cvt_pk_f16_f32 v154, v92, v93
	v_cvt_pk_f16_f32 v155, v94, v95
	ds_read_b64_tr_b16 v[70:71], v65 offset:2048
	ds_read_b64_tr_b16 v[72:73], v65 offset:2560
	s_waitcnt lgkmcnt(13)
	v_mfma_f32_32x32x16_f16 v[112:127], v[172:175], v[132:135], v[112:127]
	v_add_f32_e32 v66, v50, v66
	v_add_f32_e32 v66, v51, v66
	v_add_f32_e32 v66, v52, v66
	v_add_f32_e32 v82, v53, v66
	v_cvt_pk_f16_f32 v148, v48, v49
	v_cvt_pk_f16_f32 v149, v50, v51
	ds_read_b64_tr_b16 v[66:67], v65 offset:6144
	ds_read_b64_tr_b16 v[68:69], v65 offset:6656
	s_waitcnt lgkmcnt(14)
	v_mfma_f32_32x32x16_f16 v[96:111], v[168:171], v[132:135], v[96:111]
	v_add_f32_e32 v48, v54, v82
	v_add_f32_e32 v48, v55, v48
	v_add_f32_e32 v48, v56, v48
	v_add_f32_e32 v48, v57, v48
	v_cvt_pk_f16_f32 v150, v52, v53
	v_cvt_pk_f16_f32 v151, v54, v55
	ds_read_b64_tr_b16 v[52:53], v65 offset:3072
	ds_read_b64_tr_b16 v[54:55], v65 offset:3584
	s_waitcnt lgkmcnt(14)
	v_mfma_f32_32x32x16_f16 v[112:127], v[164:167], v[128:131], v[112:127]
	v_add_f32_e32 v48, v58, v48
	v_add_f32_e32 v48, v59, v48
	v_add_f32_e32 v48, v60, v48
	v_add_f32_e32 v82, v61, v48
	v_cvt_pk_f16_f32 v144, v56, v57
	v_cvt_pk_f16_f32 v145, v58, v59
	ds_read_b64_tr_b16 v[48:49], v65 offset:7168
	ds_read_b64_tr_b16 v[50:51], v65 offset:7680
	v_mfma_f32_32x32x16_f16 v[96:111], v[160:163], v[128:131], v[96:111]
	v_add_f32_e32 v56, v62, v82
	v_add_f32_e32 v56, v63, v56
	v_cvt_pk_f16_f32 v146, v60, v61
	v_cvt_pk_f16_f32 v147, v62, v63
	v_max_f32_e32 v57, v112, v113
	v_max3_f32 v58, v114, v115, v116
	v_max3_f32 v57, v57, v117, v118
	v_max3_f32 v58, v58, v119, v120
	v_max3_f32 v57, v57, v121, v122
	v_max3_f32 v58, v58, v123, v124
	v_max3_f32 v57, v57, v125, v126
	v_add_f32_e32 v64, v64, v56
	v_max3_f32 v58, v58, v127, v96
	v_max3_f32 v57, v57, v97, v98
	v_max3_f32 v58, v58, v99, v100
	v_max3_f32 v57, v57, v101, v102
	v_max3_f32 v58, v58, v103, v104
	v_max3_f32 v57, v57, v105, v106
	v_max3_f32 v58, v58, v107, v108
	v_max3_f32 v57, v57, v109, v110
	v_max3_f32 v56, v57, v58, v111
	v_cmp_lt_f32_e32 vcc, s17, v56
	s_cmp_lg_u64 vcc, 0
	s_cbranch_scc1 .LBB1_95
.LBB1_88:
	s_add_u32 s52, s4, 0xffffe000
	s_addc_u32 s53, s5, -1
	s_waitcnt lgkmcnt(14)
	v_mfma_f32_32x32x16_f16 v[0:15], v[156:159], v[192:195], v[0:15]
	v_exp_f32_e32 v112, v112
	v_exp_f32_e32 v113, v113
	v_exp_f32_e32 v114, v114
	v_exp_f32_e32 v115, v115
	s_add_i32 s54, s30, s22
	s_mov_b32 m0, s54
	s_waitcnt lgkmcnt(12)
	v_mfma_f32_32x32x16_f16 v[16:31], v[156:159], v[188:191], v[16:31]
	global_load_lds_dwordx4 v211, s[52:53]
	v_exp_f32_e32 v116, v116
	v_exp_f32_e32 v117, v117
	v_exp_f32_e32 v118, v118
	v_exp_f32_e32 v119, v119
	v_add_u32_e32 v60, s12, v250
	ds_read_b128 v[56:59], v60
	ds_read_b128 v[160:163], v60 offset:512
	s_add_u32 s52, s2, 0xffffe000
	s_addc_u32 s53, s3, -1
	s_add_i32 s54, s12, s23
	s_mov_b32 m0, s54
	s_waitcnt lgkmcnt(12)
	v_mfma_f32_32x32x16_f16 v[0:15], v[152:155], v[78:81], v[0:15]
	global_load_lds_dwordx4 v211, s[52:53]
	v_exp_f32_e32 v120, v120
	v_exp_f32_e32 v121, v121
	v_exp_f32_e32 v122, v122
	v_exp_f32_e32 v123, v123
	ds_read_b128 v[188:191], v60 offset:2048
	ds_read_b128 v[184:187], v60 offset:2560
	s_waitcnt lgkmcnt(12)
	v_mfma_f32_32x32x16_f16 v[16:31], v[152:155], v[74:77], v[16:31]
	v_exp_f32_e32 v124, v124
	v_exp_f32_e32 v125, v125
	v_exp_f32_e32 v126, v126
	v_exp_f32_e32 v127, v127
	ds_read_b128 v[74:77], v60 offset:4096
	ds_read_b128 v[176:179], v60 offset:4608
	s_waitcnt lgkmcnt(12)
	v_mfma_f32_32x32x16_f16 v[0:15], v[148:151], v[70:73], v[0:15]
	v_exp_f32_e32 v96, v96
	v_exp_f32_e32 v97, v97
	v_exp_f32_e32 v98, v98
	v_exp_f32_e32 v99, v99
	ds_read_b128 v[180:183], v60 offset:6144
	ds_read_b128 v[172:175], v60 offset:6656
	s_waitcnt lgkmcnt(12)
	v_mfma_f32_32x32x16_f16 v[16:31], v[148:151], v[66:69], v[16:31]
	v_exp_f32_e32 v100, v100
	v_exp_f32_e32 v101, v101
	v_exp_f32_e32 v102, v102
	v_exp_f32_e32 v103, v103
	s_waitcnt lgkmcnt(10)
	v_mfma_f32_32x32x16_f16 v[0:15], v[144:147], v[52:55], v[0:15]
	v_exp_f32_e32 v104, v104
	v_exp_f32_e32 v105, v105
	v_exp_f32_e32 v106, v106
	v_exp_f32_e32 v107, v107
	s_waitcnt lgkmcnt(8)
	v_mfma_f32_32x32x16_f16 v[16:31], v[144:147], v[48:51], v[16:31]
	v_exp_f32_e32 v108, v108
	v_exp_f32_e32 v109, v109
	v_exp_f32_e32 v110, v110
	v_exp_f32_e32 v111, v111
	s_waitcnt vmcnt(2) lgkmcnt(0)
	s_barrier
	s_andn2_b64 vcc, exec, s[6:7]
	s_cbranch_vccnz .LBB1_90
	s_waitcnt lgkmcnt(0)
	v_add_u32_e32 v65, s21, v212
	ds_read_b128 v[48:51], v65 offset:49248
	ds_read_b128 v[52:55], v65 offset:49216
	ds_read_b128 v[60:63], v65 offset:49184
	ds_read_b128 v[66:69], v65 offset:49152
	s_waitcnt lgkmcnt(3)
	v_pk_mul_f32 v[12:13], v[12:13], v[48:49]
	s_waitcnt lgkmcnt(2)
	v_pk_mul_f32 v[8:9], v[8:9], v[52:53]
	s_waitcnt lgkmcnt(1)
	v_pk_mul_f32 v[4:5], v[4:5], v[60:61]
	v_pk_mul_f32 v[14:15], v[14:15], v[50:51]
	v_pk_mul_f32 v[10:11], v[10:11], v[54:55]
	v_pk_mul_f32 v[6:7], v[6:7], v[62:63]
	s_waitcnt lgkmcnt(0)
	v_pk_mul_f32 v[2:3], v[2:3], v[68:69]
	v_pk_mul_f32 v[0:1], v[0:1], v[66:67]
	v_pk_mul_f32 v[28:29], v[28:29], v[48:49]
	v_pk_mul_f32 v[24:25], v[24:25], v[52:53]
	v_pk_mul_f32 v[20:21], v[20:21], v[60:61]
	v_pk_mul_f32 v[30:31], v[30:31], v[50:51]
	v_pk_mul_f32 v[26:27], v[26:27], v[54:55]
	v_pk_mul_f32 v[22:23], v[22:23], v[62:63]
	v_pk_mul_f32 v[18:19], v[18:19], v[68:69]
	v_pk_mul_f32 v[16:17], v[16:17], v[66:67]
.LBB1_90:
	s_add_i32 s6, s12, 0x2000
	s_cmpk_lg_i32 s12, 0x4000
	s_cselect_b32 s25, s6, 0
	v_add_u32_e32 v65, s30, v251
	ds_read_b64_tr_b16 v[168:169], v65
	ds_read_b64_tr_b16 v[170:171], v65 offset:512
	s_waitcnt lgkmcnt(9)
	v_mfma_f32_32x32x16_f16 v[80:95], v[56:59], v[140:143], v[32:47]
	s_mov_b64 s[6:7], 0
	v_add_f32_e32 v48, v112, v113
	v_add_f32_e32 v48, v114, v48
	v_add_f32_e32 v48, v115, v48
	v_add_f32_e32 v48, v116, v48
	v_add_f32_e32 v48, v117, v48
	v_cvt_pk_f16_f32 v156, v112, v113
	v_cvt_pk_f16_f32 v157, v114, v115
	ds_read_b64_tr_b16 v[164:165], v65 offset:4096
	ds_read_b64_tr_b16 v[166:167], v65 offset:4608
	v_add_f32_e32 v48, v118, v48
	v_add_f32_e32 v48, v119, v48
	v_add_f32_e32 v48, v120, v48
	v_add_f32_e32 v66, v121, v48
	s_waitcnt lgkmcnt(10)
	v_mfma_f32_32x32x16_f16 v[48:63], v[160:163], v[140:143], v[32:47]
	v_cvt_pk_f16_f32 v158, v116, v117
	v_cvt_pk_f16_f32 v159, v118, v119
	ds_read_b64_tr_b16 v[160:161], v65 offset:1024
	ds_read_b64_tr_b16 v[162:163], v65 offset:1536
	s_waitcnt lgkmcnt(11)
	v_mfma_f32_32x32x16_f16 v[80:95], v[188:191], v[136:139], v[80:95]
	v_add_f32_e32 v66, v122, v66
	v_add_f32_e32 v66, v123, v66
	v_add_f32_e32 v66, v124, v66
	v_add_f32_e32 v66, v125, v66
	v_cvt_pk_f16_f32 v152, v120, v121
	v_cvt_pk_f16_f32 v153, v122, v123
	ds_read_b64_tr_b16 v[116:117], v65 offset:5120
	ds_read_b64_tr_b16 v[118:119], v65 offset:5632
	s_waitcnt lgkmcnt(12)
	v_mfma_f32_32x32x16_f16 v[48:63], v[184:187], v[136:139], v[48:63]
	v_add_f32_e32 v66, v126, v66
	v_add_f32_e32 v66, v127, v66
	v_add_f32_e32 v66, v96, v66
	v_add_f32_e32 v66, v97, v66
	v_cvt_pk_f16_f32 v154, v124, v125
	v_cvt_pk_f16_f32 v155, v126, v127
	ds_read_b64_tr_b16 v[112:113], v65 offset:2048
	ds_read_b64_tr_b16 v[114:115], v65 offset:2560
	s_waitcnt lgkmcnt(13)
	v_mfma_f32_32x32x16_f16 v[80:95], v[74:77], v[132:135], v[80:95]
	v_add_f32_e32 v66, v98, v66
	v_add_f32_e32 v66, v99, v66
	v_add_f32_e32 v66, v100, v66
	v_add_f32_e32 v66, v101, v66
	v_cvt_pk_f16_f32 v148, v96, v97
	v_cvt_pk_f16_f32 v149, v98, v99
	ds_read_b64_tr_b16 v[74:75], v65 offset:6144
	ds_read_b64_tr_b16 v[76:77], v65 offset:6656
	s_waitcnt lgkmcnt(14)
	v_mfma_f32_32x32x16_f16 v[48:63], v[176:179], v[132:135], v[48:63]
	v_add_f32_e32 v66, v102, v66
	v_add_f32_e32 v66, v103, v66
	v_add_f32_e32 v66, v104, v66
	v_add_f32_e32 v66, v105, v66
	v_cvt_pk_f16_f32 v150, v100, v101
	v_cvt_pk_f16_f32 v151, v102, v103
	ds_read_b64_tr_b16 v[70:71], v65 offset:3072
	ds_read_b64_tr_b16 v[72:73], v65 offset:3584
	s_waitcnt lgkmcnt(14)
	v_mfma_f32_32x32x16_f16 v[80:95], v[180:183], v[128:131], v[80:95]
	v_add_f32_e32 v66, v106, v66
	v_add_f32_e32 v66, v107, v66
	v_add_f32_e32 v66, v108, v66
	v_add_f32_e32 v78, v109, v66
	v_cvt_pk_f16_f32 v144, v104, v105
	v_cvt_pk_f16_f32 v145, v106, v107
	ds_read_b64_tr_b16 v[66:67], v65 offset:7168
	ds_read_b64_tr_b16 v[68:69], v65 offset:7680
	v_mfma_f32_32x32x16_f16 v[48:63], v[172:175], v[128:131], v[48:63]
	v_add_f32_e32 v65, v110, v78
	v_add_f32_e32 v65, v111, v65
	v_cvt_pk_f16_f32 v146, v108, v109
	v_cvt_pk_f16_f32 v147, v110, v111
	v_max_f32_e32 v78, v80, v81
	v_max3_f32 v79, v82, v83, v84
	v_max3_f32 v78, v78, v85, v86
	v_max3_f32 v79, v79, v87, v88
	v_max3_f32 v78, v78, v89, v90
	v_max3_f32 v79, v79, v91, v92
	v_max3_f32 v78, v78, v93, v94
	v_add_f32_e32 v64, v64, v65
	v_max3_f32 v79, v79, v95, v48
	v_max3_f32 v78, v78, v49, v50
	v_max3_f32 v79, v79, v51, v52
	v_max3_f32 v78, v78, v53, v54
	v_max3_f32 v79, v79, v55, v56
	v_max3_f32 v78, v78, v57, v58
	v_max3_f32 v79, v79, v59, v60
	v_max3_f32 v78, v78, v61, v62
	v_max3_f32 v65, v78, v79, v63
	v_cmp_lt_f32_e32 vcc, s17, v65
	s_cmp_lg_u64 vcc, 0
	s_cbranch_scc1 .LBB1_98
.LBB1_91:
	s_add_i32 s54, s12, s22
	s_add_i32 s55, s25, s23
	s_waitcnt lgkmcnt(14)
	v_mfma_f32_32x32x16_f16 v[0:15], v[156:159], v[168:171], v[0:15]
	v_exp_f32_e32 v80, v80
	v_exp_f32_e32 v81, v81
	v_exp_f32_e32 v82, v82
	v_exp_f32_e32 v83, v83
	s_mov_b32 m0, s54
	s_waitcnt lgkmcnt(12)
	v_mfma_f32_32x32x16_f16 v[16:31], v[156:159], v[164:167], v[16:31]
	global_load_lds_dwordx4 v211, s[4:5]
	v_exp_f32_e32 v84, v84
	v_exp_f32_e32 v85, v85
	v_exp_f32_e32 v86, v86
	v_exp_f32_e32 v87, v87
	v_add_u32_e32 v65, s25, v250
	ds_read_b128 v[188:191], v65
	ds_read_b128 v[184:187], v65 offset:512
	s_mov_b32 m0, s55
	s_waitcnt lgkmcnt(12)
	v_mfma_f32_32x32x16_f16 v[0:15], v[152:155], v[160:163], v[0:15]
	global_load_lds_dwordx4 v211, s[2:3]
	v_exp_f32_e32 v88, v88
	v_exp_f32_e32 v89, v89
	v_exp_f32_e32 v90, v90
	v_exp_f32_e32 v91, v91
	ds_read_b128 v[180:183], v65 offset:2048
	ds_read_b128 v[176:179], v65 offset:2560
	s_waitcnt lgkmcnt(12)
	v_mfma_f32_32x32x16_f16 v[16:31], v[152:155], v[116:119], v[16:31]
	v_exp_f32_e32 v92, v92
	v_exp_f32_e32 v93, v93
	v_exp_f32_e32 v94, v94
	v_exp_f32_e32 v95, v95
	ds_read_b128 v[172:175], v65 offset:4096
	ds_read_b128 v[168:171], v65 offset:4608
	s_waitcnt lgkmcnt(12)
	v_mfma_f32_32x32x16_f16 v[0:15], v[148:151], v[112:115], v[0:15]
	v_exp_f32_e32 v48, v48
	v_exp_f32_e32 v49, v49
	v_exp_f32_e32 v50, v50
	v_exp_f32_e32 v51, v51
	ds_read_b128 v[164:167], v65 offset:6144
	ds_read_b128 v[160:163], v65 offset:6656
	s_waitcnt lgkmcnt(12)
	v_mfma_f32_32x32x16_f16 v[16:31], v[148:151], v[74:77], v[16:31]
	v_exp_f32_e32 v52, v52
	v_exp_f32_e32 v53, v53
	v_exp_f32_e32 v54, v54
	v_exp_f32_e32 v55, v55
	s_waitcnt lgkmcnt(10)
	v_mfma_f32_32x32x16_f16 v[0:15], v[144:147], v[70:73], v[0:15]
	v_exp_f32_e32 v56, v56
	v_exp_f32_e32 v57, v57
	v_exp_f32_e32 v58, v58
	v_exp_f32_e32 v59, v59
	s_waitcnt lgkmcnt(8)
	v_mfma_f32_32x32x16_f16 v[16:31], v[144:147], v[66:69], v[16:31]
	v_exp_f32_e32 v60, v60
	v_exp_f32_e32 v61, v61
	v_exp_f32_e32 v62, v62
	v_exp_f32_e32 v63, v63
	s_waitcnt vmcnt(2) lgkmcnt(0)
	s_barrier
	s_andn2_b64 vcc, exec, s[6:7]
	s_cbranch_vccnz .LBB1_93
	s_waitcnt lgkmcnt(0)
	v_add_u32_e32 v65, s21, v212
	ds_read_b128 v[66:69], v65 offset:49248
	ds_read_b128 v[70:73], v65 offset:49216
	ds_read_b128 v[74:77], v65 offset:49184
	ds_read_b128 v[96:99], v65 offset:49152
	s_waitcnt lgkmcnt(3)
	v_pk_mul_f32 v[12:13], v[12:13], v[66:67]
	s_waitcnt lgkmcnt(2)
	v_pk_mul_f32 v[8:9], v[8:9], v[70:71]
	s_waitcnt lgkmcnt(1)
	v_pk_mul_f32 v[4:5], v[4:5], v[74:75]
	v_pk_mul_f32 v[14:15], v[14:15], v[68:69]
	v_pk_mul_f32 v[10:11], v[10:11], v[72:73]
	v_pk_mul_f32 v[6:7], v[6:7], v[76:77]
	s_waitcnt lgkmcnt(0)
	v_pk_mul_f32 v[2:3], v[2:3], v[98:99]
	v_pk_mul_f32 v[0:1], v[0:1], v[96:97]
	v_pk_mul_f32 v[28:29], v[28:29], v[66:67]
	v_pk_mul_f32 v[24:25], v[24:25], v[70:71]
	v_pk_mul_f32 v[20:21], v[20:21], v[74:75]
	v_pk_mul_f32 v[30:31], v[30:31], v[68:69]
	v_pk_mul_f32 v[26:27], v[26:27], v[72:73]
	v_pk_mul_f32 v[22:23], v[22:23], v[76:77]
	v_pk_mul_f32 v[18:19], v[18:19], v[98:99]
	v_pk_mul_f32 v[16:17], v[16:17], v[96:97]

.LBB1_95:
	s_mov_b64 s[6:7], -1
	v_mov_b32_e32 v57, v56
	s_nop 1
	v_permlane32_swap_b32_e32 v56, v57
	v_max_f32_e32 v56, v56, v57
	v_max_f32_e32 v32, v56, v56
	v_max_f32_e32 v56, 0, v32
	v_exp_f32_e64 v57, -v56
	v_add_f32_e32 v249, v249, v56
	v_xor_b32_e32 v32, 0x80000000, v249
	v_mov_b32_e32 v33, v32
	v_mov_b32_e32 v34, v32
	v_mov_b32_e32 v35, v32
	v_mov_b32_e32 v36, v32
	v_mov_b32_e32 v37, v32
	v_mov_b32_e32 v38, v32
	v_mov_b32_e32 v39, v32
	v_mov_b32_e32 v40, v32
	v_mov_b32_e32 v41, v32
	v_mov_b32_e32 v42, v32
	v_mov_b32_e32 v43, v32
	v_mov_b32_e32 v44, v32
	v_mov_b32_e32 v45, v32
	v_mov_b32_e32 v46, v32
	v_mov_b32_e32 v47, v32
	s_and_saveexec_b64 s[8:9], s[0:1]
	ds_write_b32 v205, v57 offset:49152
	s_or_b64 exec, exec, s[8:9]
	v_sub_f32_e32 v127, v127, v56
	v_sub_f32_e32 v126, v126, v56
	v_sub_f32_e32 v125, v125, v56
	v_sub_f32_e32 v124, v124, v56
	v_sub_f32_e32 v123, v123, v56
	v_sub_f32_e32 v122, v122, v56
	v_sub_f32_e32 v121, v121, v56
	v_sub_f32_e32 v120, v120, v56
	v_sub_f32_e32 v119, v119, v56
	v_sub_f32_e32 v118, v118, v56
	v_sub_f32_e32 v117, v117, v56
	v_sub_f32_e32 v116, v116, v56
	v_sub_f32_e32 v115, v115, v56
	v_sub_f32_e32 v114, v114, v56
	v_sub_f32_e32 v113, v113, v56
	v_sub_f32_e32 v112, v112, v56
	v_sub_f32_e32 v111, v111, v56
	v_sub_f32_e32 v110, v110, v56
	v_sub_f32_e32 v109, v109, v56
	v_sub_f32_e32 v108, v108, v56
	v_sub_f32_e32 v107, v107, v56
	v_sub_f32_e32 v106, v106, v56
	v_sub_f32_e32 v105, v105, v56
	v_sub_f32_e32 v104, v104, v56
	v_sub_f32_e32 v103, v103, v56
	v_sub_f32_e32 v102, v102, v56
	v_sub_f32_e32 v101, v101, v56
	v_sub_f32_e32 v100, v100, v56
	v_sub_f32_e32 v99, v99, v56
	v_sub_f32_e32 v98, v98, v56
	v_sub_f32_e32 v97, v97, v56
	v_sub_f32_e32 v96, v96, v56
	v_mul_f32_e32 v64, v64, v57
	s_branch .LBB1_88
.LBB1_98:
	s_mov_b64 s[6:7], -1
	v_mov_b32_e32 v78, v65
	s_nop 1
	v_permlane32_swap_b32_e32 v65, v78
	v_max_f32_e32 v65, v65, v78
	v_max_f32_e32 v32, v65, v65
	v_max_f32_e32 v65, 0, v32
	v_exp_f32_e64 v78, -v65
	v_add_f32_e32 v249, v249, v65
	v_xor_b32_e32 v32, 0x80000000, v249
	v_mov_b32_e32 v33, v32
	v_mov_b32_e32 v34, v32
	v_mov_b32_e32 v35, v32
	v_mov_b32_e32 v36, v32
	v_mov_b32_e32 v37, v32
	v_mov_b32_e32 v38, v32
	v_mov_b32_e32 v39, v32
	v_mov_b32_e32 v40, v32
	v_mov_b32_e32 v41, v32
	v_mov_b32_e32 v42, v32
	v_mov_b32_e32 v43, v32
	v_mov_b32_e32 v44, v32
	v_mov_b32_e32 v45, v32
	v_mov_b32_e32 v46, v32
	v_mov_b32_e32 v47, v32
	s_and_saveexec_b64 s[8:9], s[0:1]
	ds_write_b32 v205, v78 offset:49152
	s_or_b64 exec, exec, s[8:9]
	v_sub_f32_e32 v95, v95, v65
	v_sub_f32_e32 v94, v94, v65
	v_sub_f32_e32 v93, v93, v65
	v_sub_f32_e32 v92, v92, v65
	v_sub_f32_e32 v91, v91, v65
	v_sub_f32_e32 v90, v90, v65
	v_sub_f32_e32 v89, v89, v65
	v_sub_f32_e32 v88, v88, v65
	v_sub_f32_e32 v87, v87, v65
	v_sub_f32_e32 v86, v86, v65
	v_sub_f32_e32 v85, v85, v65
	v_sub_f32_e32 v84, v84, v65
	v_sub_f32_e32 v83, v83, v65
	v_sub_f32_e32 v82, v82, v65
	v_sub_f32_e32 v81, v81, v65
	v_sub_f32_e32 v80, v80, v65
	v_sub_f32_e32 v63, v63, v65
	v_sub_f32_e32 v62, v62, v65
	v_sub_f32_e32 v61, v61, v65
	v_sub_f32_e32 v60, v60, v65
	v_sub_f32_e32 v59, v59, v65
	v_sub_f32_e32 v58, v58, v65
	v_sub_f32_e32 v57, v57, v65
	v_sub_f32_e32 v56, v56, v65
	v_sub_f32_e32 v55, v55, v65
	v_sub_f32_e32 v54, v54, v65
	v_sub_f32_e32 v53, v53, v65
	v_sub_f32_e32 v52, v52, v65
	v_sub_f32_e32 v51, v51, v65
	v_sub_f32_e32 v50, v50, v65
	v_sub_f32_e32 v49, v49, v65
	v_sub_f32_e32 v48, v48, v65
	v_mul_f32_e32 v64, v64, v78
	s_branch .LBB1_91
